# baseline (speedup 1.0000x reference)
_Z11k_conv_mfmaPKDF16_PKDv8_DF16_PKfS5_S5_S5_S5_PDF16_:
	s_load_dwordx4 s[8:11], s[0:1], 0x0
	s_load_dwordx8 s[36:43], s[0:1], 0x10
	s_load_dwordx4 s[44:47], s[0:1], 0x30
	s_lshr_b32 s6, s2, 1
	v_readfirstlane_b32 s24, v0
	s_and_b32 s25, s2, 3
	s_and_b32 s3, s6, 2
	s_lshr_b32 s4, s2, 7
	s_lshr_b32 s2, s2, 3
	s_lshr_b32 s23, s24, 6
	s_add_i32 s7, s3, s4
	s_and_b32 s22, s2, 12
	s_mul_i32 s2, s25, 0x65400
	v_and_b32_e32 v1, 63, v0
	s_waitcnt lgkmcnt(0)
	s_lshl_b32 s21, s7, 2
	s_and_b32 s20, s6, 12
	s_add_i32 s12, s20, -1
	s_add_u32 s48, s10, 0x880
	s_addc_u32 s49, s11, 0
	s_movk_i32 s26, 0xba3
	s_movk_i32 s27, 0x140
	v_add_u32_e32 v17, 64, v1
	v_add_u32_e32 v18, 0x80, v1
	v_mul_u32_u24_e32 v19, s26, v1
	v_mul_u32_u24_e32 v20, s26, v17
	v_mul_u32_u24_e32 v21, s26, v18
	v_lshrrev_b32_e32 v19, 16, v19
	v_lshrrev_b32_e32 v20, 16, v20
	v_lshrrev_b32_e32 v21, 16, v21
	v_mul_u32_u24_e32 v22, 22, v19
	v_mul_u32_u24_e32 v23, 22, v20
	v_mul_u32_u24_e32 v31, 22, v21
	v_sub_u32_e32 v22, v1, v22
	v_sub_u32_e32 v23, v17, v23
	v_sub_u32_e32 v31, v18, v31
	v_min_u32_e32 v22, 19, v22
	v_min_u32_e32 v23, 19, v23
	v_min_u32_e32 v31, 19, v31
	v_lshlrev_b32_e32 v22, 4, v22
	v_lshlrev_b32_e32 v23, 4, v23
	v_lshlrev_b32_e32 v31, 4, v31
	v_mad_u32_u24 v24, v19, s27, v22
	v_mad_u32_u24 v25, v20, s27, v23
	v_mad_u32_u24 v26, v21, s27, v31
	v_add_u32_e32 v22, s12, v19
	v_add_u32_e32 v23, s12, v20
	v_add_u32_e32 v31, s12, v21
	v_cmp_gt_u32_e64 s[14:15], 16, v22
	v_cmp_gt_u32_e64 s[16:17], 16, v23
	v_cmp_gt_u32_e64 s[18:19], 16, v31
	s_add_i32 s26, s23, 0
	s_mul_i32 s27, s26, 43
	s_lshr_b32 s27, s27, 8
	s_mul_i32 s28, s27, 6
	s_sub_i32 s28, s26, s28
	s_add_i32 s27, s27, s21
	s_add_i32 s28, s28, s22
	s_add_i32 s27, s27, -1
	s_add_i32 s28, s28, -1
	s_or_b32 s29, s27, s28
	s_lshl_b32 s27, s27, 8
	s_lshl_b32 s28, s28, 4
	s_add_i32 s27, s27, s28
	s_add_i32 s27, s27, s12
	s_mulk_i32 s27, 0x140
	s_ashr_i32 s28, s27, 31
	s_add_u32 s34, s8, s27
	s_addc_u32 s35, s9, s28
	s_sub_u32 s30, s48, s34
	s_mul_i32 s31, s26, 0x840
	s_cmp_lt_u32 s29, 16
	s_cselect_b64 s[50:51], s[14:15], 0
	s_cselect_b64 s[52:53], s[16:17], 0
	s_cselect_b64 s[54:55], s[18:19], 0
	v_mov_b32_e32 v27, s30
	v_cndmask_b32_e64 v28, v27, v24, s[50:51]
	s_mov_b32 m0, s31
	s_nop 0
	global_load_lds_dwordx4 v28, s[34:35]
	v_cndmask_b32_e64 v29, v27, v25, s[52:53]
	s_add_u32 m0, s31, 0x400
	s_nop 0
	global_load_lds_dwordx4 v29, s[34:35]
	v_cndmask_b32_e64 v30, v27, v26, s[54:55]
	s_add_u32 m0, s31, 0x800
	s_mov_b64 exec, 15
	global_load_lds_dwordx4 v30, s[34:35]
	s_mov_b64 exec, -1
	s_add_i32 s26, s23, 8
	s_mul_i32 s27, s26, 43
	s_lshr_b32 s27, s27, 8
	s_mul_i32 s28, s27, 6
	s_sub_i32 s28, s26, s28
	s_add_i32 s27, s27, s21
	s_add_i32 s28, s28, s22
	s_add_i32 s27, s27, -1
	s_add_i32 s28, s28, -1
	s_or_b32 s29, s27, s28
	s_lshl_b32 s27, s27, 8
	s_lshl_b32 s28, s28, 4
	s_add_i32 s27, s27, s28
	s_add_i32 s27, s27, s12
	s_mulk_i32 s27, 0x140
	s_ashr_i32 s28, s27, 31
	s_add_u32 s34, s8, s27
	s_addc_u32 s35, s9, s28
	s_sub_u32 s30, s48, s34
	s_mul_i32 s31, s26, 0x840
	s_cmp_lt_u32 s29, 16
	s_cselect_b64 s[50:51], s[14:15], 0
	s_cselect_b64 s[52:53], s[16:17], 0
	s_cselect_b64 s[54:55], s[18:19], 0
	v_mov_b32_e32 v27, s30
	v_cndmask_b32_e64 v28, v27, v24, s[50:51]
	s_mov_b32 m0, s31
	s_nop 0
	global_load_lds_dwordx4 v28, s[34:35]
	v_cndmask_b32_e64 v29, v27, v25, s[52:53]
	s_add_u32 m0, s31, 0x400
	s_nop 0
	global_load_lds_dwordx4 v29, s[34:35]
	v_cndmask_b32_e64 v30, v27, v26, s[54:55]
	s_add_u32 m0, s31, 0x800
	s_mov_b64 exec, 15
	global_load_lds_dwordx4 v30, s[34:35]
	s_mov_b64 exec, -1
	s_add_i32 s26, s23, 16
	s_mul_i32 s27, s26, 43
	s_lshr_b32 s27, s27, 8
	s_mul_i32 s28, s27, 6
	s_sub_i32 s28, s26, s28
	s_add_i32 s27, s27, s21
	s_add_i32 s28, s28, s22
	s_add_i32 s27, s27, -1
	s_add_i32 s28, s28, -1
	s_or_b32 s29, s27, s28
	s_lshl_b32 s27, s27, 8
	s_lshl_b32 s28, s28, 4
	s_add_i32 s27, s27, s28
	s_add_i32 s27, s27, s12
	s_mulk_i32 s27, 0x140
	s_ashr_i32 s28, s27, 31
	s_add_u32 s34, s8, s27
	s_addc_u32 s35, s9, s28
	s_sub_u32 s30, s48, s34
	s_mul_i32 s31, s26, 0x840
	s_cmp_lt_u32 s29, 16
	s_cselect_b64 s[50:51], s[14:15], 0
	s_cselect_b64 s[52:53], s[16:17], 0
	s_cselect_b64 s[54:55], s[18:19], 0
	v_mov_b32_e32 v27, s30
	v_cndmask_b32_e64 v28, v27, v24, s[50:51]
	s_mov_b32 m0, s31
	s_nop 0
	global_load_lds_dwordx4 v28, s[34:35]
	v_cndmask_b32_e64 v29, v27, v25, s[52:53]
	s_add_u32 m0, s31, 0x400
	s_nop 0
	global_load_lds_dwordx4 v29, s[34:35]
	v_cndmask_b32_e64 v30, v27, v26, s[54:55]
	s_add_u32 m0, s31, 0x800
	s_mov_b64 exec, 15
	global_load_lds_dwordx4 v30, s[34:35]
	s_mov_b64 exec, -1
	s_add_i32 s26, s23, 24
	s_mul_i32 s27, s26, 43
	s_lshr_b32 s27, s27, 8
	s_mul_i32 s28, s27, 6
	s_sub_i32 s28, s26, s28
	s_add_i32 s27, s27, s21
	s_add_i32 s28, s28, s22
	s_add_i32 s27, s27, -1
	s_add_i32 s28, s28, -1
	s_or_b32 s29, s27, s28
	s_lshl_b32 s27, s27, 8
	s_lshl_b32 s28, s28, 4
	s_add_i32 s27, s27, s28
	s_add_i32 s27, s27, s12
	s_mulk_i32 s27, 0x140
	s_ashr_i32 s28, s27, 31
	s_add_u32 s34, s8, s27
	s_addc_u32 s35, s9, s28
	s_sub_u32 s30, s48, s34
	s_mul_i32 s31, s26, 0x840
	s_cmp_lt_u32 s29, 16
	s_cselect_b64 s[50:51], s[14:15], 0
	s_cselect_b64 s[52:53], s[16:17], 0
	s_cselect_b64 s[54:55], s[18:19], 0
	v_mov_b32_e32 v27, s30
	v_cndmask_b32_e64 v28, v27, v24, s[50:51]
	s_mov_b32 m0, s31
	s_nop 0
	global_load_lds_dwordx4 v28, s[34:35]
	v_cndmask_b32_e64 v29, v27, v25, s[52:53]
	s_add_u32 m0, s31, 0x400
	s_nop 0
	global_load_lds_dwordx4 v29, s[34:35]
	v_cndmask_b32_e64 v30, v27, v26, s[54:55]
	s_add_u32 m0, s31, 0x800
	s_mov_b64 exec, 15
	global_load_lds_dwordx4 v30, s[34:35]
	s_mov_b64 exec, -1
	s_cmp_gt_u32 s23, 3
	s_cbranch_scc1 .Lmy_conv_skip4
	s_add_i32 s26, s23, 32
	s_mul_i32 s27, s26, 43
	s_lshr_b32 s27, s27, 8
	s_mul_i32 s28, s27, 6
	s_sub_i32 s28, s26, s28
	s_add_i32 s27, s27, s21
	s_add_i32 s28, s28, s22
	s_add_i32 s27, s27, -1
	s_add_i32 s28, s28, -1
	s_or_b32 s29, s27, s28
	s_lshl_b32 s27, s27, 8
	s_lshl_b32 s28, s28, 4
	s_add_i32 s27, s27, s28
	s_add_i32 s27, s27, s12
	s_mulk_i32 s27, 0x140
	s_ashr_i32 s28, s27, 31
	s_add_u32 s34, s8, s27
	s_addc_u32 s35, s9, s28
	s_sub_u32 s30, s48, s34
	s_mul_i32 s31, s26, 0x840
	s_cmp_lt_u32 s29, 16
	s_cselect_b64 s[50:51], s[14:15], 0
	s_cselect_b64 s[52:53], s[16:17], 0
	s_cselect_b64 s[54:55], s[18:19], 0
	v_mov_b32_e32 v27, s30
	v_cndmask_b32_e64 v28, v27, v24, s[50:51]
	s_mov_b32 m0, s31
	s_nop 0
	global_load_lds_dwordx4 v28, s[34:35]
	v_cndmask_b32_e64 v29, v27, v25, s[52:53]
	s_add_u32 m0, s31, 0x400
	s_nop 0
	global_load_lds_dwordx4 v29, s[34:35]
	v_cndmask_b32_e64 v30, v27, v26, s[54:55]
	s_add_u32 m0, s31, 0x800
	s_mov_b64 exec, 15
	global_load_lds_dwordx4 v30, s[34:35]
	s_mov_b64 exec, -1
.Lmy_conv_skip4:
	v_and_b32_e32 v135, 15, v0
	s_mul_i32 s25, s25, 40
	v_add_lshl_u32 v10, v135, s25, 2
	v_or_b32_e32 v11, 32, v135
	v_cmp_gt_u32_e32 vcc, 40, v11
	global_load_dword v164, v10, s[44:45]
	global_load_dword v140, v10, s[36:37]
	global_load_dword v141, v10, s[42:43]
	global_load_dword v134, v10, s[40:41]
	global_load_dword v138, v10, s[38:39] offset:64
	global_load_dword v139, v10, s[36:37] offset:64
	global_load_dword v165, v10, s[44:45] offset:64
	v_cndmask_b32_e32 v11, 0, v11, vcc
	v_add_lshl_u32 v11, v11, s25, 2
	global_load_dword v142, v11, s[36:37]
	global_load_dword v143, v11, s[42:43]
	global_load_dword v136, v11, s[40:41]
	global_load_dword v166, v11, s[44:45]
	global_load_dword v146, v10, s[38:39]
	global_load_dword v144, v11, s[38:39]
	global_load_dword v145, v10, s[42:43] offset:64
	global_load_dword v137, v10, s[40:41] offset:64
	s_add_u32 s4, s10, s2
	v_mov_b32_e32 v10, 0
	s_addc_u32 s5, s11, 0
	v_lshlrev_b32_e32 v2, 4, v1
	v_mov_b32_e32 v3, v10
	v_lshl_add_u64 v[130:131], s[4:5], 0, v[2:3]
	v_and_b32_e32 v2, 8, v0
	v_lshlrev_b32_e32 v2, 4, v2
	s_mul_i32 s2, s23, 0xc0
	s_mov_b32 s3, 0
	v_sub_co_u32_e32 v132, vcc, v130, v2
	s_ashr_i32 s5, s2, 31
	s_mov_b32 s4, s2
	v_subbrev_co_u32_e32 v133, vcc, 0, v131, vcc
	v_lshl_add_u64 v[12:13], s[2:3], 4, v[130:131]
	s_lshl_b64 s[4:5], s[4:5], 4
	v_lshl_add_u64 v[14:15], v[130:131], 0, s[4:5]
	global_load_dwordx4 v[2:5], v[12:13], off
	global_load_dwordx4 v[6:9], v[14:15], off offset:1024
	v_lshl_add_u64 v[12:13], v[132:133], 0, s[4:5]
	s_add_i32 s4, s2, 0x600
	s_mov_b32 s5, s3
	v_lshl_add_u64 v[14:15], s[4:5], 4, v[130:131]
	s_ashr_i32 s5, s4, 31
	s_lshl_b64 s[4:5], s[4:5], 4
	global_load_dwordx4 v[98:101], v[12:13], off offset:2048
	global_load_dwordx4 v[86:89], v[14:15], off
	v_lshl_add_u64 v[12:13], v[130:131], 0, s[4:5]
	v_lshl_add_u64 v[14:15], v[132:133], 0, s[4:5]
	s_add_i32 s4, s2, 0xc00
	s_mov_b32 s5, s3
	global_load_dwordx4 v[90:93], v[12:13], off offset:1024
	global_load_dwordx4 v[94:97], v[14:15], off offset:2048
	v_lshl_add_u64 v[12:13], s[4:5], 4, v[130:131]
	s_ashr_i32 s5, s4, 31
	s_lshl_b64 s[4:5], s[4:5], 4
	v_lshl_add_u64 v[14:15], v[130:131], 0, s[4:5]
	global_load_dwordx4 v[74:77], v[12:13], off
	global_load_dwordx4 v[78:81], v[14:15], off offset:1024
	v_lshl_add_u64 v[12:13], v[132:133], 0, s[4:5]
	s_add_i32 s4, s2, 0x1200
	s_mov_b32 s5, s3
	v_lshl_add_u64 v[14:15], s[4:5], 4, v[130:131]
	s_ashr_i32 s5, s4, 31
	s_lshl_b64 s[4:5], s[4:5], 4
	global_load_dwordx4 v[82:85], v[12:13], off offset:2048
	global_load_dwordx4 v[62:65], v[14:15], off
	v_lshl_add_u64 v[12:13], v[130:131], 0, s[4:5]
	s_addk_i32 s2, 0x1800
	v_lshl_add_u64 v[14:15], v[132:133], 0, s[4:5]
	global_load_dwordx4 v[66:69], v[12:13], off offset:1024
	global_load_dwordx4 v[70:73], v[14:15], off offset:2048
	v_lshl_add_u64 v[12:13], s[2:3], 4, v[130:131]
	s_ashr_i32 s3, s2, 31
	s_lshl_b64 s[2:3], s[2:3], 4
	v_lshl_add_u64 v[14:15], v[130:131], 0, s[2:3]
	global_load_dwordx4 v[50:53], v[12:13], off
	global_load_dwordx4 v[54:57], v[14:15], off offset:1024
	v_lshl_add_u64 v[12:13], v[132:133], 0, s[2:3]
	global_load_dwordx4 v[58:61], v[12:13], off offset:2048
	s_waitcnt vmcnt(15)
	s_waitcnt lgkmcnt(0)
	s_min_u32 s2, s23, 0x5e
	s_mulk_i32 s2, 0xc00
	s_mov_b32 s19, 0
	s_add_i32 s18, s2, 0x1e000
	v_lshl_add_u64 v[10:11], v[130:131], 0, s[18:19]
	v_lshl_add_u64 v[12:13], v[132:133], 0, s[18:19]
	s_barrier
	global_load_dwordx4 v[102:105], v[10:11], off
	global_load_dwordx4 v[106:109], v[10:11], off offset:1024
	global_load_dwordx4 v[110:113], v[12:13], off offset:2048
	v_and_b32_e32 v11, 3, v0
	v_bfe_u32 v12, v0, 2, 2
	s_mov_b32 s4, 0xf800000
	v_mad_u32_u24 v11, v11, 6, v12
	v_and_b32_e32 v10, 48, v0
	s_movk_i32 s18, 0x160
	v_mad_u32_u24 v150, v11, s18, v10
	v_add_f32_e32 v12, 0x3727c5ac, v164
	v_mul_f32_e32 v14, 0x4f800000, v12
	v_cmp_gt_f32_e32 vcc, s4, v12
	v_add_f32_e32 v13, 0x3727c5ac, v165
	v_mul_f32_e32 v15, 0x4f800000, v13
	v_cndmask_b32_e32 v147, v12, v14, vcc
	v_cmp_gt_f32_e64 s[2:3], s4, v13
	v_add_f32_e32 v12, 0x3727c5ac, v166
	v_cmp_gt_f32_e64 s[4:5], s4, v12
	v_cndmask_b32_e64 v148, v13, v15, s[2:3]
	v_mul_f32_e32 v13, 0x4f800000, v12
	v_sqrt_f32_e32 v154, v147
	v_cndmask_b32_e64 v149, v12, v13, s[4:5]
	v_sqrt_f32_e32 v155, v148
	v_sqrt_f32_e32 v156, v149
	v_add_u32_e32 v157, -1, v154
	v_add_u32_e32 v151, 1, v154
	v_add_u32_e32 v158, -1, v155
	v_add_u32_e32 v152, 1, v155
	v_fma_f32 v12, -v157, v154, v147
	v_fma_f32 v13, -v151, v154, v147
	v_add_u32_e32 v159, -1, v156
	v_add_u32_e32 v153, 1, v156
	v_fma_f32 v14, -v158, v155, v148
	v_fma_f32 v15, -v152, v155, v148
	v_cmp_ge_f32_e64 s[12:13], 0, v12
	v_cmp_lt_f32_e64 s[6:7], 0, v13
	v_fma_f32 v12, -v159, v156, v149
	v_fma_f32 v13, -v153, v156, v149
	v_cmp_ge_f32_e64 s[14:15], 0, v14
	v_cmp_lt_f32_e64 s[8:9], 0, v15
	v_cmp_ge_f32_e64 s[16:17], 0, v12
	v_cmp_lt_f32_e64 s[10:11], 0, v13
	s_cmpk_gt_u32 s24, 0x21bf
	s_cbranch_scc1 .LBB0_24
	s_mul_i32 s27, s23, 0x6d
	s_lshr_b32 s28, s27, 8
	s_sub_i32 s28, s23, s28
	s_bfe_u32 s28, s28, 0x70001
	s_bfe_u32 s27, s27, 0x80008
	s_add_i32 s28, s28, s27
	s_bfe_u32 s27, s28, 0x30005
	s_mul_i32 s28, s23, 0x89
	s_bfe_u32 s28, s28, 0x5000b
	s_mul_i32 s29, s28, 0x56
	s_mul_i32 s18, s23, 0xcd
	s_bfe_u32 s29, s29, 0x80008
	s_bfe_u32 s18, s18, 0x6000a
	s_mul_i32 s29, s29, 3
	s_sub_i32 s28, s28, s29
	s_mul_i32 s29, s18, 0x56
	s_bfe_u32 s29, s29, 0x80008
	s_mul_i32 s29, s29, 3
	s_mul_i32 s26, s18, -5
	s_sub_i32 s18, s18, s29
	s_mul_i32 s27, s27, 36
	s_mul_i32 s28, s28, 6
	s_or_b32 s18, s18, s27
	s_add_i32 s18, s18, s28
	s_add_i32 s26, s26, s23
	s_and_b32 s18, s18, 0xff
	s_mulk_i32 s18, 0x160
	s_lshl_b32 s26, s26, 6
	s_add_i32 s26, s26, s18
	v_add_u32_e32 v14, s26, v150
	ds_read_b128 v[10:13], v14
	ds_read_b128 v[114:117], v14 offset:38016
	s_waitcnt lgkmcnt(1)
	v_mfma_f32_16x16x32_f16 v[46:49], v[10:13], v[2:5], 0
	v_mfma_f32_16x16x32_f16 v[42:45], v[10:13], v[6:9], 0
	v_mfma_f32_16x16x32_f16 v[34:37], v[10:13], v[98:101], 0
	ds_read_b128 v[10:13], v14 offset:12672
	ds_read_b128 v[14:17], v14 offset:25344
	s_waitcnt lgkmcnt(1)
	v_mfma_f32_16x16x32_f16 v[38:41], v[10:13], v[2:5], 0
	v_mfma_f32_16x16x32_f16 v[30:33], v[10:13], v[6:9], 0
	v_mfma_f32_16x16x32_f16 v[26:29], v[10:13], v[98:101], 0
	s_waitcnt lgkmcnt(0)
	v_mfma_f32_16x16x32_f16 v[22:25], v[14:17], v[2:5], 0
	v_mfma_f32_16x16x32_f16 v[18:21], v[14:17], v[6:9], 0
	v_mfma_f32_16x16x32_f16 v[14:17], v[14:17], v[98:101], 0
	v_mfma_f32_16x16x32_f16 v[10:13], v[114:117], v[2:5], 0
	v_mfma_f32_16x16x32_f16 v[6:9], v[114:117], v[6:9], 0
	v_mfma_f32_16x16x32_f16 v[2:5], v[114:117], v[98:101], 0
	s_branch .LBB0_25
